# mLSTM level-1 state update: the 18 V^T fragment LDS reads issued 12 ahead into distinct register quads with counted lgkmcnt waits (was one quad, lgkmcnt(0) before every MFMA)
# baseline (speedup 1.0000x reference)
.LBB0_426:
	v_mul_f32_e32 v62, s15, v221
	ds_read_b128 v[50:53], v124 offset:34816
	ds_read_b128 v[46:49], v124 offset:34880
	v_exp_f32_e32 v62, v62
	ds_read_b128 v[172:175], v119 offset:53248
	ds_read_b128 v[176:179], v119 offset:53312
	ds_read_b128 v[180:183], v119 offset:55552
	ds_read_b128 v[184:187], v119 offset:55616
	ds_read_b128 v[188:191], v119 offset:57856
	ds_read_b128 v[192:195], v119 offset:57920
	ds_read_b128 v[196:199], v119 offset:60160
	ds_read_b128 v[200:203], v119 offset:60224
	ds_read_b128 v[204:207], v119 offset:62464
	ds_read_b128 v[226:229], v119 offset:62528
	ds_read_b128 v[230:233], v119 offset:64768
	ds_read_b128 v[234:237], v119 offset:64832
	s_add_i32 s14, s14, 64
	v_add_f32_e32 v100, s15, v100
	v_pk_mul_f32 v[40:41], v[40:41], v[62:63] op_sel_hi:[1,0]
	v_pk_mul_f32 v[38:39], v[38:39], v[62:63] op_sel_hi:[1,0]
	v_pk_mul_f32 v[44:45], v[44:45], v[62:63] op_sel_hi:[1,0]
	v_pk_mul_f32 v[42:43], v[42:43], v[62:63] op_sel_hi:[1,0]
	v_pk_mul_f32 v[36:37], v[36:37], v[62:63] op_sel_hi:[1,0]
	v_pk_mul_f32 v[34:35], v[34:35], v[62:63] op_sel_hi:[1,0]
	v_pk_mul_f32 v[32:33], v[32:33], v[62:63] op_sel_hi:[1,0]
	v_pk_mul_f32 v[30:31], v[30:31], v[62:63] op_sel_hi:[1,0]
	v_pk_mul_f32 v[28:29], v[28:29], v[62:63] op_sel_hi:[1,0]
	v_pk_mul_f32 v[26:27], v[26:27], v[62:63] op_sel_hi:[1,0]
	v_pk_mul_f32 v[24:25], v[24:25], v[62:63] op_sel_hi:[1,0]
	v_pk_mul_f32 v[22:23], v[22:23], v[62:63] op_sel_hi:[1,0]
	v_pk_mul_f32 v[20:21], v[20:21], v[62:63] op_sel_hi:[1,0]
	v_pk_mul_f32 v[18:19], v[18:19], v[62:63] op_sel_hi:[1,0]
	v_pk_mul_f32 v[16:17], v[16:17], v[62:63] op_sel_hi:[1,0]
	v_pk_mul_f32 v[14:15], v[14:15], v[62:63] op_sel_hi:[1,0]
	v_pk_mul_f32 v[12:13], v[12:13], v[62:63] op_sel_hi:[1,0]
	v_pk_mul_f32 v[10:11], v[10:11], v[62:63] op_sel_hi:[1,0]
	v_add_u32_e32 v122, 0x200, v122
	s_cmpk_eq_i32 s14, 0x200
	s_waitcnt lgkmcnt(11)
	v_mfma_f32_16x16x32_bf16 v[38:41], v[50:53], v[172:175], v[38:41]
	ds_read_b128 v[238:241], v120 offset:13824
	s_waitcnt lgkmcnt(11)
	v_mfma_f32_16x16x32_bf16 v[38:41], v[46:49], v[176:179], v[38:41]
	ds_read_b128 v[242:245], v120 offset:13888
	s_waitcnt lgkmcnt(11)
	v_mfma_f32_16x16x32_bf16 v[42:45], v[50:53], v[180:183], v[42:45]
	ds_read_b128 v[246:249], v120 offset:16128
	s_waitcnt lgkmcnt(11)
	v_mfma_f32_16x16x32_bf16 v[42:45], v[46:49], v[184:187], v[42:45]
	ds_read_b128 v[154:157], v120 offset:16192
	s_waitcnt lgkmcnt(11)
	v_mfma_f32_16x16x32_bf16 v[34:37], v[50:53], v[188:191], v[34:37]
	ds_read_b128 v[158:161], v120 offset:18432
	s_waitcnt lgkmcnt(11)
	v_mfma_f32_16x16x32_bf16 v[34:37], v[46:49], v[192:195], v[34:37]
	ds_read_b128 v[162:165], v120 offset:18496
	s_waitcnt lgkmcnt(11)
	v_mfma_f32_16x16x32_bf16 v[30:33], v[50:53], v[196:199], v[30:33]
	s_waitcnt lgkmcnt(10)
	v_mfma_f32_16x16x32_bf16 v[30:33], v[46:49], v[200:203], v[30:33]
	s_waitcnt lgkmcnt(9)
	v_mfma_f32_16x16x32_bf16 v[26:29], v[50:53], v[204:207], v[26:29]
	s_waitcnt lgkmcnt(8)
	v_mfma_f32_16x16x32_bf16 v[26:29], v[46:49], v[226:229], v[26:29]
	s_waitcnt lgkmcnt(7)
	v_mfma_f32_16x16x32_bf16 v[22:25], v[50:53], v[230:233], v[22:25]
	s_waitcnt lgkmcnt(6)
	v_mfma_f32_16x16x32_bf16 v[22:25], v[46:49], v[234:237], v[22:25]
	s_waitcnt lgkmcnt(5)
	v_mfma_f32_16x16x32_bf16 v[18:21], v[50:53], v[238:241], v[18:21]
	s_waitcnt lgkmcnt(4)
	v_mfma_f32_16x16x32_bf16 v[18:21], v[46:49], v[242:245], v[18:21]
	s_waitcnt lgkmcnt(3)
	v_mfma_f32_16x16x32_bf16 v[14:17], v[50:53], v[246:249], v[14:17]
	s_waitcnt lgkmcnt(2)
	v_mfma_f32_16x16x32_bf16 v[14:17], v[46:49], v[154:157], v[14:17]
	s_waitcnt lgkmcnt(1)
	v_mfma_f32_16x16x32_bf16 v[10:13], v[50:53], v[158:161], v[10:13]
	s_waitcnt lgkmcnt(0)
	s_barrier
	v_mfma_f32_16x16x32_bf16 v[10:13], v[46:49], v[162:165], v[10:13]
	s_cbranch_scc1 .LBB0_431
